# P6 and P9 per-row-block setup loops de-serialised (all 12/8 loads issued before first wait), on top of sc1/nt policy variant
# speedup vs baseline: 1.0017x; 1.0009x over previous
.LBB0_1183:
	s_waitcnt vmcnt(10)
	v_add_u32_e32 v7, s4, v5
	v_add_u32_e32 v6, 0x1a00, v7
	v_add_u32_e32 v8, 0x2200, v7
	v_ashrrev_i32_e32 v7, 31, v6
	v_ashrrev_i32_e32 v9, 31, v8
	v_lshl_add_u64 v[6:7], v[6:7], 2, s[74:75]
	v_lshl_add_u64 v[8:9], v[8:9], 2, s[74:75]
	global_load_dword v20, v[6:7], off
	global_load_dword v21, v[8:9], off
	global_load_dword v22, v[2:3], off
	global_load_dword v23, v[6:7], off offset:2048
	global_load_dword v24, v[8:9], off offset:2048
	global_load_dword v25, v[2:3], off offset:2048
	v_lshl_add_u64 v[10:11], v[6:7], 0, s[22:23]
	v_lshl_add_u64 v[12:13], v[8:9], 0, s[22:23]
	v_lshl_add_u64 v[14:15], v[2:3], 0, s[22:23]
	v_lshl_add_u64 v[10:11], v[10:11], 0, s[22:23]
	v_lshl_add_u64 v[12:13], v[12:13], 0, s[22:23]
	v_lshl_add_u64 v[14:15], v[14:15], 0, s[22:23]
	global_load_dword v26, v[10:11], off
	global_load_dword v27, v[12:13], off
	global_load_dword v28, v[14:15], off
	global_load_dword v29, v[10:11], off offset:2048
	global_load_dword v30, v[12:13], off offset:2048
	global_load_dword v31, v[14:15], off offset:2048
	s_waitcnt vmcnt(9)
	v_add_f32_e32 v21, 1.0, v21
	v_mul_f32_e32 v21, v21, v22
	ds_write2st64_b32 v4, v20, v21 offset1:32
	s_waitcnt vmcnt(6)
	v_add_f32_e32 v24, 1.0, v24
	v_mul_f32_e32 v24, v24, v25
	ds_write2st64_b32 v4, v23, v24 offset0:8 offset1:40
	s_waitcnt vmcnt(3)
	v_add_f32_e32 v27, 1.0, v27
	v_mul_f32_e32 v27, v27, v28
	ds_write2st64_b32 v4, v26, v27 offset0:16 offset1:48
	s_waitcnt vmcnt(0)
	v_add_f32_e32 v30, 1.0, v30
	v_mul_f32_e32 v30, v30, v31
	ds_write2st64_b32 v4, v29, v30 offset0:24 offset1:56
	s_or_b64 exec, exec, s[0:1]
	s_and_saveexec_b64 s[0:1], s[2:3]
	ds_write_b32 v200, v103 offset:41472
	s_or_b64 exec, exec, s[0:1]
	s_lshl_b32 s48, s47, 6
	s_add_i32 s48, s48, s33
	v_or_b32_e32 v2, s48, v198
	v_ashrrev_i32_e32 v3, 31, v2
	v_lshl_add_u64 v[4:5], v[2:3], 2, s[20:21]
	v_add_co_u32_e32 v6, vcc, s39, v4
	s_waitcnt lgkmcnt(0)
	s_nop 0
	v_addc_co_u32_e32 v7, vcc, 0, v5, vcc
	v_add_co_u32_e32 v8, vcc, s36, v4
	s_barrier
	s_nop 0
	v_addc_co_u32_e32 v9, vcc, 0, v5, vcc
	v_add_co_u32_e32 v10, vcc, s34, v4
	s_nop 1
	v_addc_co_u32_e32 v11, vcc, 0, v5, vcc
	v_add_co_u32_e32 v12, vcc, s40, v4
	v_lshlrev_b64 v[2:3], 13, v[2:3]
	s_nop 0
	v_addc_co_u32_e32 v13, vcc, 0, v5, vcc
	v_add_co_u32_e32 v14, vcc, s41, v4
	v_lshl_add_u64 v[54:55], v[116:117], 0, v[2:3]
	s_nop 0
	v_addc_co_u32_e32 v15, vcc, 0, v5, vcc
	v_add_co_u32_e32 v16, vcc, s42, v4
	v_ashrrev_i32_e32 v121, 31, v120
	s_nop 0
	v_addc_co_u32_e32 v17, vcc, 0, v5, vcc
	v_add_co_u32_e32 v18, vcc, s43, v4
	v_mad_i64_i32 v[150:151], s[0:1], v120, s38, v[102:103]
	s_nop 0
	v_addc_co_u32_e32 v19, vcc, 0, v5, vcc
	global_load_dword v58, v[4:5], off
	global_load_dword v59, v[6:7], off
	global_load_dword v60, v[8:9], off
	global_load_dword v61, v[10:11], off
	global_load_dword v62, v[12:13], off
	global_load_dword v63, v[14:15], off
	global_load_dword v64, v[16:17], off
	global_load_dword v65, v[18:19], off
	global_load_dwordx4 v[46:49], v[104:105], off
	global_load_dwordx4 v[26:29], v[106:107], off
	global_load_dwordx4 v[22:25], v[108:109], off
	s_nop 0
	global_load_dwordx4 v[18:21], v[110:111], off
	global_load_dwordx4 v[14:17], v[112:113], off
	global_load_dwordx4 v[10:13], v[114:115], off
	global_load_dwordx4 v[2:5], v[54:55], off offset:16
	global_load_dwordx4 v[6:9], v[54:55], off
	global_load_dwordx4 v[30:33], v[54:55], off offset:144
	global_load_dwordx4 v[34:37], v[54:55], off offset:128
	global_load_dwordx4 v[38:41], v[54:55], off offset:272
	global_load_dwordx4 v[42:45], v[54:55], off offset:256
	global_load_dwordx4 v[50:53], v[54:55], off offset:400
	s_nop 0
	global_load_dwordx4 v[54:57], v[54:55], off offset:384
	v_mad_i64_i32 v[152:153], s[0:1], v120, s38, v[122:123]
	v_mad_i64_i32 v[154:155], s[0:1], v120, s38, v[124:125]
	v_mad_i64_i32 v[156:157], s[0:1], v120, s38, v[126:127]
	v_mad_i64_i32 v[158:159], s[0:1], v120, s38, v[142:143]
	v_mad_i64_i32 v[160:161], s[0:1], v120, s38, v[144:145]
	v_mad_i64_i32 v[162:163], s[0:1], v120, s38, v[146:147]
	v_mad_i64_i32 v[164:165], s[0:1], v120, s38, v[148:149]
	v_mov_b32_e32 v90, 0
	s_mov_b32 s0, -2
	v_mov_b64_e32 v[166:167], v[140:141]
	v_mov_b64_e32 v[168:169], v[138:139]
	v_mov_b64_e32 v[170:171], v[136:137]
	v_mov_b64_e32 v[172:173], v[134:135]
	v_mov_b64_e32 v[182:183], v[132:133]
	v_mov_b64_e32 v[184:185], v[130:131]
	v_mov_b32_e32 v91, v90
	v_mov_b32_e32 v92, v90
	v_mov_b32_e32 v93, v90
	v_mov_b32_e32 v98, v90
	v_mov_b32_e32 v99, v90
	v_mov_b32_e32 v100, v90
	v_mov_b32_e32 v101, v90
	v_mov_b32_e32 v94, v90
	v_mov_b32_e32 v95, v90
	v_mov_b32_e32 v96, v90
	v_mov_b32_e32 v97, v90
	s_waitcnt vmcnt(21)
	v_add_f32_e32 v58, 0, v58
	s_waitcnt vmcnt(20)
	v_add_f32_e32 v58, v58, v59
	s_waitcnt vmcnt(19)
	v_add_f32_e32 v58, v58, v60
	s_waitcnt vmcnt(18)
	v_add_f32_e32 v58, v58, v61
	s_waitcnt vmcnt(17)
	v_add_f32_e32 v58, v58, v62
	s_waitcnt vmcnt(16)
	v_add_f32_e32 v58, v58, v63
	s_waitcnt vmcnt(15)
	v_add_f32_e32 v58, v58, v64
	s_waitcnt vmcnt(14)
	v_add_f32_e32 v58, v58, v65
	v_fmamk_f32 v58, v58, 0x3a000000, v203
	v_mul_f32_e32 v59, 0x4b800000, v58
	v_cmp_gt_f32_e32 vcc, s44, v58
	s_nop 1
	v_cndmask_b32_e32 v58, v58, v59, vcc
	v_rsq_f32_e32 v60, v58
	v_lshlrev_b64 v[58:59], 13, v[120:121]
	v_lshl_add_u64 v[174:175], v[128:129], 0, v[58:59]
	v_mov_b32_e32 v121, v202
	v_mul_f32_e32 v58, 0x45800000, v60
	v_cndmask_b32_e32 v176, v60, v58, vcc
	v_mov_b32_e32 v177, v176
	v_mov_b32_e32 v180, v176
	v_mov_b32_e32 v181, v176
	s_branch .LBB0_1188

.LBB0_1490:
	v_add_u32_e32 v4, s3, v3
	v_add_u32_e32 v4, 0x2a00, v4
	v_ashrrev_i32_e32 v5, 31, v4
	v_lshl_add_u64 v[4:5], v[4:5], 2, s[74:75]
	global_load_dword v6, v[0:1], off
	global_load_dword v7, v[4:5], off
	global_load_dword v8, v[0:1], off offset:2048
	global_load_dword v9, v[4:5], off offset:2048
	v_lshl_add_u64 v[10:11], v[0:1], 0, s[6:7]
	v_lshl_add_u64 v[12:13], v[4:5], 0, s[6:7]
	v_lshl_add_u64 v[10:11], v[10:11], 0, s[6:7]
	v_lshl_add_u64 v[12:13], v[12:13], 0, s[6:7]
	global_load_dword v14, v[10:11], off
	global_load_dword v15, v[12:13], off
	global_load_dword v16, v[10:11], off offset:2048
	global_load_dword v17, v[12:13], off offset:2048
	s_waitcnt vmcnt(6)
	ds_write2st64_b32 v2, v7, v6 offset1:32
	s_waitcnt vmcnt(4)
	ds_write2st64_b32 v2, v9, v8 offset0:8 offset1:40
	s_waitcnt vmcnt(2)
	ds_write2st64_b32 v2, v15, v14 offset0:16 offset1:48
	s_waitcnt vmcnt(0)
	ds_write2st64_b32 v2, v17, v16 offset0:24 offset1:56
	s_or_b64 exec, exec, s[0:1]
	s_ashr_i32 s5, s4, 31
	s_mul_i32 s1, s4, 0x9000
	s_mul_hi_i32 s0, s4, 0x9000
	s_add_u32 s10, s96, s1
	s_addc_u32 s11, s97, s0
	s_lshl_b64 s[0:1], s[4:5], 13
	s_add_u32 s14, s78, s0
	s_addc_u32 s15, s79, s1
	s_ashr_i32 s3, s2, 31
	s_lshl_b64 s[0:1], s[2:3], 13
	s_add_u32 s16, s78, s0
	s_addc_u32 s17, s79, s1
	s_mul_i32 s1, s2, 0x9000
	s_mul_hi_i32 s0, s2, 0x9000
	s_add_u32 s18, s96, s1
	s_addc_u32 s19, s97, s0
	s_mov_b32 s3, -2
	s_mov_b32 s5, 0
	s_waitcnt lgkmcnt(0)
	s_barrier
